# v016 + NA ring last-q-step wait fix (halo loads now covered by vmcnt(0) when the q prefetch is skipped)
# speedup vs baseline: 1.0215x; 1.0061x over previous
; #define LAS __attribute__((address_space(3)))
; __device__ __forceinline__ void na_ring(const Params& p, LAS unsigned char* lds, int unit) {
;     ...
;     for (int r = 0; r < 32; ++r) {
;         const int r0 = min(max(r - 4, 0), 24);
;         const bool pf = (r >= 4) && (r < 28);
;         u32x4 pk_ = {0u, 0u, 0u, 0u}, pv_ = {0u, 0u, 0u, 0u};
;         if (pf) { pk_ = *(const u32x4*)(kg + (size_t)(r + 4) * 64 * LD0); pv_ = *(const u32x4*)(vg + (r + 4) * 64); }
;         bf16x8 qn0 = qf[0], qn1 = qf[1];
;         if (r + 1 < 32) { qn0 = *(const bf16x8*)(qg + (size_t)(r + 1) * 64 * LD0); qn1 = *(const bf16x8*)(qg + (size_t)(r + 1) * 64 * LD0 + 32); }
;     ...
;         if (pf) { const int sl = (r + 4) % 9; *(LAS u32x4*)(lds + KRING + sl * 8192 + st_off) = pk_; *(LAS u32x4*)(lds + VRING + sl * 8192 + st_off) = pv_; }
;         __syncthreads();
.Lna_last_q:
	s_waitcnt vmcnt(0)
	s_branch .LBB0_304
